# static s_setprio 1 for waves 0-3 during the ten GEMM phases, per-segment flips removed, on top of the barrier change
# speedup vs baseline: 1.0164x; 1.0164x over previous
; #define MKCTX() Ctx C; { int t_ = tid_from_wave(wave_s); asm volatile("" : "+v"(t_)); C.lds = (LAS unsigned char*)lds_raw; C.tid = t_; C.lane = t_ & 63; C.wave = __builtin_amdgcn_readfirstlane(t_ >> 6); \
;         C.G = gridDim.x; const int bx_ = blockIdx.x; C.vcu = (C.G % 8 == 0) ? (bx_ % 8) * (C.G / 8) + bx_ / 8 : bx_; C.gw = C.vcu * NWAVES + C.wave; C.NGW = C.G * NWAVES; }
; __global__ void __launch_bounds__(NWAVES * 64, 2) fwd(Args args) {
;     ...
;     if (IN(2)) for (int rep_ = 0; rep_ < NREP(2); ++rep_) { MKCTX(); pg8::Gemm g{HN, (const bf16*)(ws + WS_WIN0), NTOK, EVEN_IN, DM / 2}; pg8::StaticOrder S; S.init(NTOK, EVEN_IN, C.G, (int)blockIdx.x);
;         pg8::EpiProj0I E{PROJ, EVEN_IN, QS_EVEN, (const float*)(ws + WS_SA), ctl + CW_CM0}; pg8::gemm_phase<pg8::EpiProj0I, pg8::StaticOrder, true, true, false, true>(C.lds, g, S, E, wave_s);
.LBB0_227:
	s_cmp_lt_i32 s94, 3
	s_cselect_b64 s[0:1], -1, 0
	s_add_u32 s58, s92, 0x9800000
	s_addc_u32 s59, s93, 0
	s_add_u32 s24, s92, 0xd800000
	s_addc_u32 s25, s93, 0
	s_and_b64 s[6:7], s[0:1], s[2:3]
	s_andn2_b64 vcc, exec, s[6:7]
	s_cbranch_vccnz .LBB0_288
	s_cmp_ge_u32 s96, 0x100
	s_cbranch_scc1 .Lsp_2
	s_setprio 1

; #define CLK1(k) do { if (MK_CLKPH == (k) && wave_s == 0) { const unsigned long long c1_ = __builtin_amdgcn_s_memtime(), r1_ = __builtin_amdgcn_s_memrealtime(); CLKW[2] = MK_CLKDUR ? (r1_ - CLKW[1]) / 10ull : (c1_ - CLKW[0]) * 100ull / (r1_ - CLKW[1]); } } while (0)
; #define MKCTX() Ctx C; { int t_ = tid_from_wave(wave_s); asm volatile("" : "+v"(t_)); C.lds = (LAS unsigned char*)lds_raw; C.tid = t_; C.lane = t_ & 63; C.wave = __builtin_amdgcn_readfirstlane(t_ >> 6); \
;         C.G = gridDim.x; const int bx_ = blockIdx.x; C.vcu = (C.G % 8 == 0) ? (bx_ % 8) * (C.G / 8) + bx_ / 8 : bx_; C.gw = C.vcu * NWAVES + C.wave; C.NGW = C.G * NWAVES; }
; #define SEAM(k) do { if (!MK_PER_PHASE && IN(k) && IN((k) + 1)) xcd_barrier(bar); } while (0)
; __global__ void __launch_bounds__(NWAVES * 64, 2) fwd(Args args) {
;     ...
;     if (IN(4)) for (int rep_ = 0; rep_ < NREP(4); ++rep_) { MKCTX(); pg8::Gemm g{MIX0, (const bf16*)(ws + WS_WO0), NTOK, DM, DM}; pg8::StaticOrder S; S.init(NTOK, DM, C.G, (int)blockIdx.x);
;         pg8::EpiResGateH<true> E{I.x, hbuf, DM, mod0 + 2 * DM, ADA, SEQ, 1.0f}; pg8::gemm_phase<pg8::EpiResGateH<true>, pg8::StaticOrder, true, true>(C.lds, g, S, E, wave_s); } if (!MK_CLKDUR) CLK1(4); SEAM(4); if (MK_CLKDUR) CLK1(4);
.LBB0_438:
	s_cmp_lt_i32 s94, 5
	s_cselect_b64 s[2:3], -1, 0
	s_add_u32 s60, s92, 0x5800000
	s_addc_u32 s61, s93, 0
	s_and_b64 s[0:1], s[2:3], s[0:1]
	s_andn2_b64 vcc, exec, s[0:1]
	s_cbranch_vccnz .LBB0_460
	s_cmp_ge_u32 s96, 0x100
	s_cbranch_scc1 .Lsp_4
	s_setprio 1

; #define CLK1(k) do { if (MK_CLKPH == (k) && wave_s == 0) { const unsigned long long c1_ = __builtin_amdgcn_s_memtime(), r1_ = __builtin_amdgcn_s_memrealtime(); CLKW[2] = MK_CLKDUR ? (r1_ - CLKW[1]) / 10ull : (c1_ - CLKW[0]) * 100ull / (r1_ - CLKW[1]); } } while (0)
; #define MKCTX() Ctx C; { int t_ = tid_from_wave(wave_s); asm volatile("" : "+v"(t_)); C.lds = (LAS unsigned char*)lds_raw; C.tid = t_; C.lane = t_ & 63; C.wave = __builtin_amdgcn_readfirstlane(t_ >> 6); \
;         C.G = gridDim.x; const int bx_ = blockIdx.x; C.vcu = (C.G % 8 == 0) ? (bx_ % 8) * (C.G / 8) + bx_ / 8 : bx_; C.gw = C.vcu * NWAVES + C.wave; C.NGW = C.G * NWAVES; }
; #define SEAM(k) do { if (!MK_PER_PHASE && IN(k) && IN((k) + 1)) xcd_barrier(bar); } while (0)
; __global__ void __launch_bounds__(NWAVES * 64, 2) fwd(Args args) {
;     ...
;     if (IN(6)) for (int rep_ = 0; rep_ < NREP(6); ++rep_) { MKCTX(); pg8::Gemm g{HN, (const bf16*)(ws + WS_WGU0), NTOK, 2 * FF, DM / 2}; pg8::StaticOrder S; S.init(NTOK, 2 * FF, C.G, (int)blockIdx.x);
;         pg8::EpiSwiGLUI8 E{(unsigned char*)ACT, FF, (const float*)(ws + WS_SA), ctl + CW_CMG}; pg8::gemm_phase<pg8::EpiSwiGLUI8, pg8::StaticOrder, true, true, false, true>(C.lds, g, S, E, wave_s); } if (!MK_CLKDUR) CLK1(6); SEAM(6); if (MK_CLKDUR) CLK1(6);
.LBB0_580:
	s_cmp_lt_i32 s94, 7
	s_cselect_b64 s[0:1], -1, 0
	s_and_b64 s[0:1], s[0:1], s[2:3]
	s_andn2_b64 vcc, exec, s[0:1]
	s_cbranch_vccnz .LBB0_598
	s_cmp_ge_u32 s96, 0x100
	s_cbranch_scc1 .Lsp_6
	s_setprio 1

; #define CLK1(k) do { if (MK_CLKPH == (k) && wave_s == 0) { const unsigned long long c1_ = __builtin_amdgcn_s_memtime(), r1_ = __builtin_amdgcn_s_memrealtime(); CLKW[2] = MK_CLKDUR ? (r1_ - CLKW[1]) / 10ull : (c1_ - CLKW[0]) * 100ull / (r1_ - CLKW[1]); } } while (0)
; #define MKCTX() Ctx C; { int t_ = tid_from_wave(wave_s); asm volatile("" : "+v"(t_)); C.lds = (LAS unsigned char*)lds_raw; C.tid = t_; C.lane = t_ & 63; C.wave = __builtin_amdgcn_readfirstlane(t_ >> 6); \
;         C.G = gridDim.x; const int bx_ = blockIdx.x; C.vcu = (C.G % 8 == 0) ? (bx_ % 8) * (C.G / 8) + bx_ / 8 : bx_; C.gw = C.vcu * NWAVES + C.wave; C.NGW = C.G * NWAVES; }
; #define SEAM(k) do { if (!MK_PER_PHASE && IN(k) && IN((k) + 1)) xcd_barrier(bar); } while (0)
; __global__ void __launch_bounds__(NWAVES * 64, 2) fwd(Args args) {
;     ...
;     if (IN(7)) for (int rep_ = 0; rep_ < NREP(7); ++rep_) { MKCTX(); pg8::Gemm g{ACT, (const bf16*)(ws + WS_WD0), NTOK, DM, FF / 2}; pg8::StaticOrder S; S.init(NTOK, DM, C.G, (int)blockIdx.x);
;         pg8::EpiResGateH<false> E{hbuf, hbuf, DM, mod0 + 5 * DM, ADA, SEQ, 1.0f / WSC_D}; pg8::gemm_phase<pg8::EpiResGateH<false>, pg8::StaticOrder, true, true, true>(C.lds, g, S, E, wave_s); } if (!MK_CLKDUR) CLK1(7); SEAM(7); if (MK_CLKDUR) CLK1(7);
.LBB0_652:
	s_cmp_lt_i32 s94, 8
	s_cselect_b64 s[0:1], -1, 0
	s_and_b64 s[0:1], s[0:1], s[2:3]
	s_andn2_b64 vcc, exec, s[0:1]
	s_cbranch_vccnz .LBB0_678
	s_cmp_ge_u32 s96, 0x100
	s_cbranch_scc1 .Lsp_7
	s_setprio 1

; #define CLK1(k) do { if (MK_CLKPH == (k) && wave_s == 0) { const unsigned long long c1_ = __builtin_amdgcn_s_memtime(), r1_ = __builtin_amdgcn_s_memrealtime(); CLKW[2] = MK_CLKDUR ? (r1_ - CLKW[1]) / 10ull : (c1_ - CLKW[0]) * 100ull / (r1_ - CLKW[1]); } } while (0)
; #define MKCTX() Ctx C; { int t_ = tid_from_wave(wave_s); asm volatile("" : "+v"(t_)); C.lds = (LAS unsigned char*)lds_raw; C.tid = t_; C.lane = t_ & 63; C.wave = __builtin_amdgcn_readfirstlane(t_ >> 6); \
;         C.G = gridDim.x; const int bx_ = blockIdx.x; C.vcu = (C.G % 8 == 0) ? (bx_ % 8) * (C.G / 8) + bx_ / 8 : bx_; C.gw = C.vcu * NWAVES + C.wave; C.NGW = C.G * NWAVES; }
; #define SEAM(k) do { if (!MK_PER_PHASE && IN(k) && IN((k) + 1)) xcd_barrier(bar); } while (0)
; __global__ void __launch_bounds__(NWAVES * 64, 2) fwd(Args args) {
;     ...
;     if (IN(9)) for (int rep_ = 0; rep_ < NREP(9); ++rep_) { MKCTX(); pg8::Gemm g{HN, (const bf16*)(ws + WS_WIN1), NTOK, ODD_IN_PAD, DM / 2}; pg8::StaticOrder S; S.init(NTOK, ODD_IN_PAD, C.G, (int)blockIdx.x);
;         pg8::EpiBf16PlainI E{PROJ, ODD_IN_PAD, (const float*)(ws + WS_SA), ctl + CW_CM1}; pg8::gemm_phase<pg8::EpiBf16PlainI, pg8::StaticOrder, true, true, false, true>(C.lds, g, S, E, wave_s); } if (!MK_CLKDUR) CLK1(9); SEAM(9); if (MK_CLKDUR) CLK1(9);
.LBB0_798:
	s_cmp_lt_i32 s94, 10
	s_cselect_b64 s[0:1], -1, 0
	s_and_b64 s[0:1], s[0:1], s[2:3]
	s_andn2_b64 vcc, exec, s[0:1]
	s_cbranch_vccnz .LBB0_816
	s_cmp_ge_u32 s96, 0x100
	s_cbranch_scc1 .Lsp_9
	s_setprio 1

; #define MKCTX() Ctx C; { int t_ = tid_from_wave(wave_s); asm volatile("" : "+v"(t_)); C.lds = (LAS unsigned char*)lds_raw; C.tid = t_; C.lane = t_ & 63; C.wave = __builtin_amdgcn_readfirstlane(t_ >> 6); \
;         C.G = gridDim.x; const int bx_ = blockIdx.x; C.vcu = (C.G % 8 == 0) ? (bx_ % 8) * (C.G / 8) + bx_ / 8 : bx_; C.gw = C.vcu * NWAVES + C.wave; C.NGW = C.G * NWAVES; }
; __global__ void __launch_bounds__(NWAVES * 64, 2) fwd(Args args) {
;     ...
;     if (IN(11)) for (int rep_ = 0; rep_ < NREP(11); ++rep_) { MKCTX();
;         { pg8::Gemm g{QN, (const bf16*)(ws + WS_WQB), NTOK, 768, 512}; pg8::StaticOrder S; S.init(NTOK, 768, C.G, (int)blockIdx.x);
;           pg8::EpiQRope E{Q, 768, ctab, stab, QS_ODD, SEQ - 1}; pg8::gemm_phase<pg8::EpiQRope, pg8::StaticOrder, true, true>(C.lds, g, S, E, wave_s); }
;         { pg8::Gemm g{KVN, (const bf16*)(ws + WS_WKVB), NTOK, 1024, 256}; pg8::StaticOrder S; S.init(NTOK, 1024, C.G, (int)blockIdx.x, (C.G == 256) ? 128 : 0);
.LBB0_954:
	s_cmp_lt_i32 s94, 12
	s_cselect_b64 s[0:1], -1, 0
	s_add_u32 s6, s92, 0x10800000
	s_addc_u32 s7, s93, 0
	s_and_b64 s[12:13], s[0:1], s[2:3]
	s_andn2_b64 vcc, exec, s[12:13]
	s_cbranch_vccnz .LBB0_1025
	s_cmp_ge_u32 s96, 0x100
	s_cbranch_scc1 .Lsp_11
	s_setprio 1

; #define CLK1(k) do { if (MK_CLKPH == (k) && wave_s == 0) { const unsigned long long c1_ = __builtin_amdgcn_s_memtime(), r1_ = __builtin_amdgcn_s_memrealtime(); CLKW[2] = MK_CLKDUR ? (r1_ - CLKW[1]) / 10ull : (c1_ - CLKW[0]) * 100ull / (r1_ - CLKW[1]); } } while (0)
; #define MKCTX() Ctx C; { int t_ = tid_from_wave(wave_s); asm volatile("" : "+v"(t_)); C.lds = (LAS unsigned char*)lds_raw; C.tid = t_; C.lane = t_ & 63; C.wave = __builtin_amdgcn_readfirstlane(t_ >> 6); \
;         C.G = gridDim.x; const int bx_ = blockIdx.x; C.vcu = (C.G % 8 == 0) ? (bx_ % 8) * (C.G / 8) + bx_ / 8 : bx_; C.gw = C.vcu * NWAVES + C.wave; C.NGW = C.G * NWAVES; }
; #define SEAM(k) do { if (!MK_PER_PHASE && IN(k) && IN((k) + 1)) xcd_barrier(bar); } while (0)
; __global__ void __launch_bounds__(NWAVES * 64, 2) fwd(Args args) {
;     ...
;     if (IN(13)) for (int rep_ = 0; rep_ < NREP(13); ++rep_) { MKCTX(); pg8::Gemm g{MIX1, (const bf16*)(ws + WS_WO1), NTOK, DM, DM}; pg8::StaticOrder S; S.init(NTOK, DM, C.G, (int)blockIdx.x);
;         pg8::EpiResGateH<false> E{hbuf, hbuf, DM, mod1 + 2 * DM, ADA, SEQ, 1.0f}; pg8::gemm_phase<pg8::EpiResGateH<false>, pg8::StaticOrder, true, true>(C.lds, g, S, E, wave_s); } if (!MK_CLKDUR) CLK1(13); SEAM(13); if (MK_CLKDUR) CLK1(13);
.LBB0_1289:
	s_cmp_lt_i32 s94, 14
	s_cselect_b64 s[2:3], -1, 0
	s_and_b64 s[0:1], s[2:3], s[0:1]
	s_andn2_b64 vcc, exec, s[0:1]
	s_cbranch_vccnz .LBB0_1311
	s_cmp_ge_u32 s96, 0x100
	s_cbranch_scc1 .Lsp_13
	s_setprio 1

; #define MKCTX() Ctx C; { int t_ = tid_from_wave(wave_s); asm volatile("" : "+v"(t_)); C.lds = (LAS unsigned char*)lds_raw; C.tid = t_; C.lane = t_ & 63; C.wave = __builtin_amdgcn_readfirstlane(t_ >> 6); \
;         C.G = gridDim.x; const int bx_ = blockIdx.x; C.vcu = (C.G % 8 == 0) ? (bx_ % 8) * (C.G / 8) + bx_ / 8 : bx_; C.gw = C.vcu * NWAVES + C.wave; C.NGW = C.G * NWAVES; }
; __global__ void __launch_bounds__(NWAVES * 64, 2) fwd(Args args) {
;     ...
;     if (IN(16)) for (int rep_ = 0; rep_ < NREP(16); ++rep_) { MKCTX();
;         const int P = __builtin_amdgcn_readfirstlane(pexp[272]);
;         pg8::MoeOrder<28, false> S{C.G, C.vcu, 0, P * 28, pexp, 0};
;         pg8::Gemm g{(const bf16*)XS, (const bf16*)(ws + WS_WEGU), 0, 0, DM / 2};
.LBB0_1505:
	s_cmp_lt_i32 s94, 17
	s_cselect_b64 s[2:3], -1, 0
	s_add_u32 s4, s92, 0x11c00000
	s_addc_u32 s5, s93, 0
	s_and_b64 s[0:1], s[2:3], s[0:1]
	s_andn2_b64 vcc, exec, s[0:1]
	s_cbranch_vccnz .LBB0_1547
	s_cmp_ge_u32 s96, 0x100
	s_cbranch_scc1 .Lsp_16
	s_setprio 1

; #define MKCTX() Ctx C; { int t_ = tid_from_wave(wave_s); asm volatile("" : "+v"(t_)); C.lds = (LAS unsigned char*)lds_raw; C.tid = t_; C.lane = t_ & 63; C.wave = __builtin_amdgcn_readfirstlane(t_ >> 6); \
;         C.G = gridDim.x; const int bx_ = blockIdx.x; C.vcu = (C.G % 8 == 0) ? (bx_ % 8) * (C.G / 8) + bx_ / 8 : bx_; C.gw = C.vcu * NWAVES + C.wave; C.NGW = C.G * NWAVES; }
; __global__ void __launch_bounds__(NWAVES * 64, 2) fwd(Args args) {
;     ...
;     if (IN(17)) for (int rep_ = 0; rep_ < NREP(17); ++rep_) { MKCTX();
;         const int P = __builtin_amdgcn_readfirstlane(pexp[272]); const int nfull = (P * 4 / C.G) * C.G;
;         pg8::MoeOrder<4, false> S{C.G, C.vcu, 0, nfull, pexp, 0};
;         pg8::Gemm g{(const bf16*)ACTE, (const bf16*)(ws + WS_WED), 0, 0, FFE / 2};
;         pg8::EpiBf16Plain E{YB, DM, 1.0f / WSC_D}; pg8::gemm_phase<pg8::EpiBf16Plain, pg8::MoeOrder<4, false>, true, true, true>(C.lds, g, S, E, wave_s);
.LBB0_1605:
	s_cmp_lt_i32 s94, 18
	s_cselect_b64 s[0:1], -1, 0
	s_and_b64 s[0:1], s[0:1], s[2:3]
	s_andn2_b64 vcc, exec, s[0:1]
	s_cbranch_vccnz .LBB0_1628
	s_cmp_ge_u32 s96, 0x100
	s_cbranch_scc1 .Lsp_17
	s_setprio 1

; #define MKCTX() Ctx C; { int t_ = tid_from_wave(wave_s); asm volatile("" : "+v"(t_)); C.lds = (LAS unsigned char*)lds_raw; C.tid = t_; C.lane = t_ & 63; C.wave = __builtin_amdgcn_readfirstlane(t_ >> 6); \
;         C.G = gridDim.x; const int bx_ = blockIdx.x; C.vcu = (C.G % 8 == 0) ? (bx_ % 8) * (C.G / 8) + bx_ / 8 : bx_; C.gw = C.vcu * NWAVES + C.wave; C.NGW = C.G * NWAVES; }
; __global__ void __launch_bounds__(NWAVES * 64, 2) fwd(Args args) {
;     ...
;     if (IN(18)) { MKCTX();
;         const int P = __builtin_amdgcn_readfirstlane(pexp[272]); const int nfull = (P * 4 / C.G) * C.G, nleft = P * 4 - nfull;
;         if (C.vcu < nleft) {
;             pg8::MoeOrder<4, false> S{C.G, C.vcu, 0, P * 4, pexp, nfull};
;             pg8::Gemm g{(const bf16*)ACTE, (const bf16*)(ws + WS_WED), 0, 0, FFE / 2};
;             pg8::EpiBf16Plain E{YB, DM, 1.0f / WSC_D}; pg8::gemm_phase<pg8::EpiBf16Plain, pg8::MoeOrder<4, false>, true, true, true>(C.lds, g, S, E, wave_s);
.LBB0_1682:
	s_cmp_lt_i32 s94, 19
	s_cselect_b64 s[0:1], -1, 0
	s_and_b64 s[0:1], s[0:1], s[2:3]
	s_andn2_b64 vcc, exec, s[0:1]
	s_cbranch_vccnz .LBB0_1725
	s_cmp_ge_u32 s96, 0x100
	s_cbranch_scc1 .Lsp_18
	s_setprio 1
